# attention inst1: K/V LDS-DMA of the next tile issued between the QK MFMAs instead of at the loop top (plus K swizzle fix)
# speedup vs baseline: 1.0016x; 1.0016x over previous
.LBB0_805:
	s_add_i32 s56, s12, -1
	s_waitcnt vmcnt(0)
	s_and_b32 s87, s56, 1
	s_xor_b32 s94, s87, 1
	s_lshl_b32 s95, s94, 14
	s_mulk_i32 s94, 0x6000
	s_add_i32 s94, s94, s64
	s_add_i32 s94, s94, 0x8000
	s_add_i32 s95, s95, s64
	s_cmp_ge_u32 s12, s85
	s_waitcnt vmcnt(0) lgkmcnt(0)
	s_barrier
	s_cbranch_scc1 .Latt1_qk_nodma
	s_mul_i32 s56, s87, 0x6000
	s_add_i32 s56, s56, 0
	s_add_i32 s56, s56, 0x8000
	v_add_u32_e32 v175, s56, v161
	ds_read_b128 v[66:69], v175 offset:0
	ds_read_b128 v[70:73], v175 offset:0x3000
	v_add_u32_e32 v200, s56, v169
	ds_read_b128 v[176:179], v200 offset:0
	ds_read_b128 v[180:183], v200 offset:0x3000
	v_add_u32_e32 v201, s56, v170
	ds_read_b128 v[184:187], v201 offset:0
	ds_read_b128 v[188:191], v201 offset:0x3000
	s_waitcnt lgkmcnt(4)
	v_add_u32_e32 v202, s56, v171
	v_mfma_f32_32x32x16_bf16 v[82:97], v[66:69], v[98:101], 0
	ds_read_b128 v[192:195], v202 offset:0
	ds_read_b128 v[196:199], v202 offset:0x3000
	s_waitcnt lgkmcnt(4)
	v_mfma_f32_32x32x16_bf16 v[66:81], v[70:73], v[98:101], 0
	s_mov_b32 m0, s94
	v_lshl_add_u64 v[204:205], s[2:3], 0, v[158:159]
	global_load_lds_dwordx4 v[204:205], off
	v_mfma_f32_32x32x16_bf16 v[82:97], v[176:179], v[102:105], v[82:97]
	ds_read_b128 v[176:179], v175 offset:0x80
	v_mfma_f32_32x32x16_bf16 v[66:81], v[180:183], v[102:105], v[66:81]
	ds_read_b128 v[180:183], v175 offset:0x3080
	s_waitcnt lgkmcnt(4)
	v_mfma_f32_32x32x16_bf16 v[82:97], v[184:187], v[106:109], v[82:97]
	ds_read_b128 v[184:187], v200 offset:0x80
	v_mfma_f32_32x32x16_bf16 v[66:81], v[188:191], v[106:109], v[66:81]
	s_add_i32 m0, s94, 0x2000
	v_lshl_add_u64 v[204:205], s[2:3], 0, v[156:157]
	global_load_lds_dwordx4 v[204:205], off
	ds_read_b128 v[188:191], v200 offset:0x3080
	s_waitcnt lgkmcnt(4)
	v_mfma_f32_32x32x16_bf16 v[82:97], v[192:195], v[110:113], v[82:97]
	ds_read_b128 v[192:195], v201 offset:0x80
	v_mfma_f32_32x32x16_bf16 v[66:81], v[196:199], v[110:113], v[66:81]
	ds_read_b128 v[196:199], v201 offset:0x3080
	s_waitcnt lgkmcnt(4)
	v_mfma_f32_32x32x16_bf16 v[82:97], v[176:179], v[114:117], v[82:97]
	ds_read_b128 v[176:179], v202 offset:0x80
	v_mfma_f32_32x32x16_bf16 v[66:81], v[180:183], v[114:117], v[66:81]
	s_add_i32 m0, s94, 0x4000
	v_lshl_add_u64 v[204:205], s[2:3], 0, v[154:155]
	global_load_lds_dwordx4 v[204:205], off
	ds_read_b128 v[180:183], v202 offset:0x3080
	s_waitcnt lgkmcnt(4)
	v_mfma_f32_32x32x16_bf16 v[82:97], v[184:187], v[118:121], v[82:97]
	ds_read_b128 v[184:187], v175 offset:0x100
	v_mfma_f32_32x32x16_bf16 v[66:81], v[188:191], v[118:121], v[66:81]
	ds_read_b128 v[188:191], v175 offset:0x3100
	s_waitcnt lgkmcnt(4)
	v_mfma_f32_32x32x16_bf16 v[82:97], v[192:195], v[122:125], v[82:97]
	ds_read_b128 v[192:195], v200 offset:0x100
	v_mfma_f32_32x32x16_bf16 v[66:81], v[196:199], v[122:125], v[66:81]
	s_mov_b32 m0, s95
	v_lshl_add_u64 v[204:205], s[2:3], 0, v[152:153]
	global_load_lds_dwordx4 v[204:205], off
	ds_read_b128 v[196:199], v200 offset:0x3100
	s_waitcnt lgkmcnt(4)
	v_mfma_f32_32x32x16_bf16 v[82:97], v[176:179], v[126:129], v[82:97]
	ds_read_b128 v[176:179], v201 offset:0x100
	v_mfma_f32_32x32x16_bf16 v[66:81], v[180:183], v[126:129], v[66:81]
	ds_read_b128 v[180:183], v201 offset:0x3100
	s_waitcnt lgkmcnt(4)
	v_mfma_f32_32x32x16_bf16 v[82:97], v[184:187], v[130:133], v[82:97]
	ds_read_b128 v[184:187], v202 offset:0x100
	v_mfma_f32_32x32x16_bf16 v[66:81], v[188:191], v[130:133], v[66:81]
	s_add_i32 m0, s95, 0x2000
	v_lshl_add_u64 v[204:205], s[2:3], 0, v[150:151]
	global_load_lds_dwordx4 v[204:205], off
	ds_read_b128 v[188:191], v202 offset:0x3100
	s_waitcnt lgkmcnt(4)
	v_mfma_f32_32x32x16_bf16 v[82:97], v[192:195], v[134:137], v[82:97]
	s_waitcnt lgkmcnt(2)
	v_mfma_f32_32x32x16_bf16 v[66:81], v[196:199], v[134:137], v[66:81]
	v_mfma_f32_32x32x16_bf16 v[82:97], v[176:179], v[138:141], v[82:97]
	s_waitcnt lgkmcnt(0)
	v_mfma_f32_32x32x16_bf16 v[66:81], v[180:183], v[138:141], v[66:81]
	v_mfma_f32_32x32x16_bf16 v[82:97], v[184:187], v[142:145], v[82:97]
	s_add_i32 s56, s86, 0x13f
	s_cmp_le_i32 s56, s84
	v_mfma_f32_32x32x16_bf16 v[66:81], v[188:191], v[142:145], v[66:81]
	s_cbranch_scc1 .LBB0_809
	s_branch .Latt1_mask

.Latt1_mask:
	v_add_u32_e32 v175, s83, v168
	v_cmp_lt_i32_e32 vcc, -1, v175
	v_add_u32_e32 v176, -1, v175
	s_nop 4
	v_cndmask_b32_e32 v82, v165, v82, vcc
	v_cmp_lt_i32_e32 vcc, 31, v175
	s_nop 1
	v_cndmask_b32_e32 v66, v165, v66, vcc
	v_cmp_lt_i32_e32 vcc, -1, v176
	s_nop 1
	v_cndmask_b32_e32 v83, v165, v83, vcc
	v_cmp_lt_i32_e32 vcc, 31, v176
	v_add_u32_e32 v176, -2, v175
	s_nop 0
	v_cndmask_b32_e32 v67, v165, v67, vcc
	v_cmp_lt_i32_e32 vcc, -1, v176
	s_nop 1
	v_cndmask_b32_e32 v84, v165, v84, vcc
	v_cmp_lt_i32_e32 vcc, 31, v176
	v_add_u32_e32 v176, -3, v175
	s_nop 0
	v_cndmask_b32_e32 v68, v165, v68, vcc
	v_cmp_lt_i32_e32 vcc, -1, v176
	s_nop 1
	v_cndmask_b32_e32 v85, v165, v85, vcc
	v_cmp_lt_i32_e32 vcc, 31, v176
	v_add_u32_e32 v176, -8, v175
	s_nop 0
	v_cndmask_b32_e32 v69, v165, v69, vcc
	v_cmp_lt_i32_e32 vcc, -1, v176
	s_nop 1
	v_cndmask_b32_e32 v86, v165, v86, vcc
	v_cmp_lt_i32_e32 vcc, 31, v176
	v_add_u32_e32 v176, -9, v175
	s_nop 0
	v_cndmask_b32_e32 v70, v165, v70, vcc
	v_cmp_lt_i32_e32 vcc, -1, v176
	s_nop 1
	v_cndmask_b32_e32 v87, v165, v87, vcc
	v_cmp_lt_i32_e32 vcc, 31, v176
	v_add_u32_e32 v176, -10, v175
	s_nop 0
	v_cndmask_b32_e32 v71, v165, v71, vcc
	v_cmp_lt_i32_e32 vcc, -1, v176
	s_nop 1
	v_cndmask_b32_e32 v88, v165, v88, vcc
	v_cmp_lt_i32_e32 vcc, 31, v176
	v_add_u32_e32 v176, -11, v175
	s_nop 0
	v_cndmask_b32_e32 v72, v165, v72, vcc
	v_cmp_lt_i32_e32 vcc, -1, v176
	s_nop 1
	v_cndmask_b32_e32 v89, v165, v89, vcc
	v_cmp_lt_i32_e32 vcc, 31, v176
	v_add_u32_e32 v176, -16, v175
	s_nop 0
	v_cndmask_b32_e32 v73, v165, v73, vcc
	v_cmp_lt_i32_e32 vcc, -1, v176
	s_nop 1
	v_cndmask_b32_e32 v90, v165, v90, vcc
	v_cmp_lt_i32_e32 vcc, 31, v176
	v_subrev_u32_e32 v176, 17, v175
	s_nop 0
	v_cndmask_b32_e32 v74, v165, v74, vcc
	v_cmp_lt_i32_e32 vcc, -1, v176
	s_nop 1
	v_cndmask_b32_e32 v91, v165, v91, vcc
	v_cmp_lt_i32_e32 vcc, 31, v176
	v_subrev_u32_e32 v176, 18, v175
	s_nop 0
	v_cndmask_b32_e32 v75, v165, v75, vcc
	v_cmp_lt_i32_e32 vcc, -1, v176
	s_nop 1
	v_cndmask_b32_e32 v92, v165, v92, vcc
	v_cmp_lt_i32_e32 vcc, 31, v176
	v_subrev_u32_e32 v176, 19, v175
	s_nop 0
	v_cndmask_b32_e32 v76, v165, v76, vcc
	v_cmp_lt_i32_e32 vcc, -1, v176
	s_nop 1
	v_cndmask_b32_e32 v93, v165, v93, vcc
	v_cmp_lt_i32_e32 vcc, 31, v176
	v_subrev_u32_e32 v176, 24, v175
	s_nop 0
	v_cndmask_b32_e32 v77, v165, v77, vcc
	v_cmp_lt_i32_e32 vcc, -1, v176
	s_nop 1
	v_cndmask_b32_e32 v94, v165, v94, vcc
	v_cmp_lt_i32_e32 vcc, 31, v176
	v_subrev_u32_e32 v176, 25, v175
	s_nop 0
	v_cndmask_b32_e32 v78, v165, v78, vcc
	v_cmp_lt_i32_e32 vcc, -1, v176
	s_nop 1
	v_cndmask_b32_e32 v95, v165, v95, vcc
	v_cmp_lt_i32_e32 vcc, 31, v176
	v_subrev_u32_e32 v176, 26, v175
	v_subrev_u32_e32 v175, 27, v175
	v_cndmask_b32_e32 v79, v165, v79, vcc
	v_cmp_lt_i32_e32 vcc, -1, v176
	s_nop 1
	v_cndmask_b32_e32 v96, v165, v96, vcc
	v_cmp_lt_i32_e32 vcc, 31, v176
	s_nop 1
	v_cndmask_b32_e32 v80, v165, v80, vcc
	v_cmp_lt_i32_e32 vcc, -1, v175
	s_nop 1
	v_cndmask_b32_e32 v97, v165, v97, vcc
	v_cmp_lt_i32_e32 vcc, 31, v175
	s_nop 1
	v_cndmask_b32_e32 v81, v165, v81, vcc
